# v12: + SG deal by DPP lane-parallel min; expert tables reused from LDS in down/combine phases
# speedup vs baseline: 1.0094x; 1.0070x over previous
; __device__ __forceinline__ void fox_phase(const Frame& F, char* lds, int& sg_first, int& sg_count) {
;     ...
;         { const int wt = Wwin / 64 + 4; int load[8], cnt[8];
; #pragma unroll
;           for (int i = 0; i < 8; ++i) { const int f0 = 4 * (i + 1), f1 = 4 * (16 - i); load[i] = (f0 < wt ? f0 : wt) + (f1 < wt ? f1 : wt); cnt[i] = 0; }
;           for (int k = 0; k < 32; ++k) { int bi = 0, bv = load[0];
; #pragma unroll
;               for (int i = 1; i < 8; ++i) if (load[i] < bv) { bv = load[i]; bi = i; }
; #pragma unroll
;               for (int i = 0; i < 8; ++i) if (i == bi) { load[i] += 8; cnt[i] += 1; } }
;           int first = 0, mine = 0;
; #pragma unroll
;           for (int i = 0; i < 8; ++i) { if (i < x) first += cnt[i]; if (i == x) mine = cnt[i]; }
;           sg_first = bh * 32 + first; sg_count = mine; }
.LBB0_799:
	s_or_b64 exec, exec, s[0:1]
	s_add_i32 s0, s9, 4
	v_and_b32_e32 v2, 7, v198
	v_lshlrev_b32_e32 v3, 2, v2
	v_add_u32_e32 v4, 4, v3
	v_sub_u32_e32 v5, 64, v3
	v_min_i32_e32 v4, s0, v4
	v_min_i32_e32 v5, s0, v5
	v_add_u32_e32 v4, v4, v5
	v_lshl_add_u32 v4, v4, 3, v2
	v_mov_b32_e32 v1, 0
	s_mov_b32 s7, 32
	s_waitcnt lgkmcnt(0)
	s_waitcnt vmcnt(63) expcnt(7) lgkmcnt(15)
	s_barrier
.Lsg_deal:
	s_nop 1
	v_min_u32_dpp v5, v4, v4 quad_perm:[1,0,3,2] row_mask:0xf bank_mask:0xf
	s_nop 1
	v_min_u32_dpp v5, v5, v5 quad_perm:[2,3,0,1] row_mask:0xf bank_mask:0xf
	s_nop 1
	v_min_u32_dpp v5, v5, v5 row_half_mirror row_mask:0xf bank_mask:0xf
	s_add_i32 s7, s7, -1
	s_cmp_lg_u32 s7, 0
	v_cmp_eq_u32_e32 vcc, v5, v4
	v_add_u32_e32 v6, 64, v4
	v_add_u32_e32 v7, 1, v1
	v_cndmask_b32_e32 v4, v4, v6, vcc
	v_cndmask_b32_e32 v1, v1, v7, vcc
	s_cbranch_scc1 .Lsg_deal
	v_cmp_gt_u32_e32 vcc, s23, v2
	s_nop 1
	v_readlane_b32 s1, v1, s23
	v_cndmask_b32_e32 v6, 0, v1, vcc
	s_nop 1
	v_add_u32_dpp v7, v6, v6 quad_perm:[1,0,3,2] row_mask:0xf bank_mask:0xf
	s_nop 1
	v_add_u32_dpp v7, v7, v7 quad_perm:[2,3,0,1] row_mask:0xf bank_mask:0xf
	s_nop 1
	v_add_u32_dpp v7, v7, v7 row_half_mirror row_mask:0xf bank_mask:0xf
	s_lshl_b32 s0, s8, 5
	v_mov_b32_e32 v1, s1
	v_readfirstlane_b32 s2, v7
	s_add_i32 s70, s0, s2
	v_cmp_gt_i32_e32 vcc, 1, v1
	s_cbranch_vccnz .LBB0_821

; #define LAS __attribute__((address_space(3)))
; __device__ __forceinline__ void moe_tables(const Frame& F) {
;     LAS int* tab = (LAS int*)(F.lds + LDS_TAB);
;     __syncthreads();
;     if (F.tid < 64) {
;         const unsigned* CNT = F.ctl + CW_CNT; const int e = F.tid & 31;
;         const int c = (int)__hip_atomic_load(CNT + e, __ATOMIC_RELAXED, __HIP_MEMORY_SCOPE_AGENT);
;         const int nt = (c + 255) >> 8; int inc = nt;
; #pragma unroll
;         for (int o = 1; o < 32; o <<= 1) { const int n = __shfl_up(inc, o); if (e >= o) inc += n; }
;         if (F.tid < 32) { tab[e] = inc - nt; tab[40 + e] = c; if (e == 31) tab[32] = inc;
;             for (int t = inc - nt; t < inc; ++t) tab[256 + t] = e; } }
;     __syncthreads();
; }
; __global__ void __launch_bounds__(NTHREADS, 2) mega_fwd(KArgs args) {
;     ...
;     if (IN(11)) {
;         moe_tables(F);
.LBB0_1988:
	s_cmp_lt_i32 s4, 12
	s_cselect_b64 s[0:1], -1, 0
	s_cmp_gt_i32 s5, 11
	s_cselect_b64 s[2:3], -1, 0
	s_and_b64 s[0:1], s[0:1], s[2:3]
	s_andn2_b64 vcc, exec, s[0:1]
	s_cbranch_vccnz .LBB0_2079
	s_cmp_gt_i32 s4, 10
	s_cselect_b32 s2, 64, 0
	v_cmp_gt_u32_e32 vcc, s2, v0
	s_waitcnt vmcnt(0) lgkmcnt(0)
	s_barrier
	s_and_saveexec_b64 s[0:1], vcc
	s_cbranch_execz .LBB0_2006
	v_and_b32_e32 v1, 31, v0
	v_lshlrev_b32_e32 v2, 2, v1
	v_mov_b32_e32 v3, 0
	v_lshl_add_u64 v[2:3], s[72:73], 0, v[2:3]
	v_add_co_u32_e32 v2, vcc, 0x8000, v2
	s_nop 1
	v_addc_co_u32_e32 v3, vcc, 0, v3, vcc
	global_load_dword v4, v[2:3], off sc1
	v_mbcnt_lo_u32_b32 v2, -1, 0
	v_mbcnt_hi_u32_b32 v2, -1, v2
	v_and_b32_e32 v3, 64, v2
	v_add_u32_e32 v5, -1, v2
	v_cmp_lt_i32_e32 vcc, v5, v3
	v_add_u32_e32 v7, -2, v2
	v_add_u32_e32 v8, -4, v2
	v_cndmask_b32_e32 v5, v5, v2, vcc
	v_lshlrev_b32_e32 v5, 2, v5
	v_cmp_lt_i32_e32 vcc, v7, v3
	v_add_u32_e32 v9, -8, v2
	v_add_u32_e32 v11, -16, v2
	v_cndmask_b32_e32 v7, v7, v2, vcc
	v_cmp_ne_u32_e32 vcc, 0, v1
	v_lshlrev_b32_e32 v7, 2, v7
	s_waitcnt vmcnt(0)
	v_add_u32_e32 v6, 0xff, v4
	v_ashrrev_i32_e32 v6, 8, v6
	ds_bpermute_b32 v5, v5, v6
	s_waitcnt lgkmcnt(0)
	v_cndmask_b32_e32 v5, 0, v5, vcc
	v_add_u32_e32 v10, v5, v6
	ds_bpermute_b32 v7, v7, v10
	v_cmp_lt_i32_e32 vcc, v8, v3
	s_nop 1
	v_cndmask_b32_e32 v8, v8, v2, vcc
	v_cmp_lt_u32_e32 vcc, 1, v1
	v_lshlrev_b32_e32 v8, 2, v8
	s_waitcnt lgkmcnt(0)
	v_cndmask_b32_e32 v7, 0, v7, vcc
	v_add_u32_e32 v10, v7, v10
	ds_bpermute_b32 v8, v8, v10
	v_cmp_lt_i32_e32 vcc, v9, v3
	s_nop 1
	v_cndmask_b32_e32 v9, v9, v2, vcc
	v_cmp_lt_u32_e32 vcc, 3, v1
	v_lshlrev_b32_e32 v9, 2, v9
	s_waitcnt lgkmcnt(0)
	v_cndmask_b32_e32 v8, 0, v8, vcc
	v_add_u32_e32 v10, v8, v10
	ds_bpermute_b32 v9, v9, v10
	v_cmp_lt_i32_e32 vcc, v11, v3
	s_nop 1
	v_cndmask_b32_e32 v3, v11, v2, vcc
	v_cmp_lt_u32_e32 vcc, 7, v1
	v_lshlrev_b32_e32 v3, 2, v3
	s_waitcnt lgkmcnt(0)
	v_cndmask_b32_e32 v9, 0, v9, vcc
	v_add_u32_e32 v2, v9, v10
	ds_bpermute_b32 v3, v3, v2
	v_cmp_gt_u32_e32 vcc, 32, v0
	s_and_b64 exec, exec, vcc
	s_cbranch_execz .LBB0_2006
	v_cmp_lt_u32_e32 vcc, 15, v1
	v_lshl_add_u32 v11, v1, 2, 0
	v_add_u32_e32 v11, 0x20100, v11
	s_waitcnt lgkmcnt(0)
	v_cndmask_b32_e32 v10, 0, v3, vcc
	v_add_u32_e32 v2, v10, v2
	v_sub_u32_e32 v3, v2, v6
	v_cmp_eq_u32_e32 vcc, 31, v1
	ds_write2_b32 v11, v3, v4 offset1:40
	s_and_saveexec_b64 s[2:3], vcc
	s_add_i32 s4, 0, 0x20180
	v_mov_b32_e32 v4, s4
	ds_write_b32 v4, v2
	s_or_b64 exec, exec, s[2:3]
	v_cmp_lt_i32_e32 vcc, 0, v6
	s_and_b64 exec, exec, vcc
	s_cbranch_execz .LBB0_2006
	v_add3_u32 v4, v5, v7, v8
	v_add3_u32 v4, v4, v9, v10
	v_add_u32_e32 v5, 1, v4
	v_max_i32_e32 v5, v2, v5
	v_sub_u32_e32 v4, v5, v4
	v_cmp_lt_u32_e32 vcc, 1, v4
	s_mov_b64 s[4:5], -1
	s_and_saveexec_b64 s[2:3], vcc
	s_cbranch_execz .LBB0_2003
	v_add_u32_e32 v6, -2, v4
	v_lshrrev_b32_e32 v5, 1, v6
	v_add_u32_e32 v5, 1, v5
	v_cmp_lt_u32_e32 vcc, 13, v6
	v_mov_b32_e32 v8, 0
	s_and_saveexec_b64 s[4:5], vcc
	s_cbranch_execz .LBB0_1999
	v_lshl_add_u32 v7, v3, 2, 0
	v_and_b32_e32 v6, -8, v5
	s_mov_b32 s8, 0
	v_add_u32_e32 v7, 0x20500, v7
	s_mov_b64 s[6:7], 0

; #define LAS __attribute__((address_space(3)))
; __device__ __forceinline__ void moe_tables(const Frame& F) {
;     LAS int* tab = (LAS int*)(F.lds + LDS_TAB);
;     __syncthreads();
;     if (F.tid < 64) {
;         const unsigned* CNT = F.ctl + CW_CNT; const int e = F.tid & 31;
;         const int c = (int)__hip_atomic_load(CNT + e, __ATOMIC_RELAXED, __HIP_MEMORY_SCOPE_AGENT);
;         const int nt = (c + 255) >> 8; int inc = nt;
; #pragma unroll
;         for (int o = 1; o < 32; o <<= 1) { const int n = __shfl_up(inc, o); if (e >= o) inc += n; }
;         if (F.tid < 32) { tab[e] = inc - nt; tab[40 + e] = c; if (e == 31) tab[32] = inc;
;             for (int t = inc - nt; t < inc; ++t) tab[256 + t] = e; } }
;     __syncthreads();
; }
; __global__ void __launch_bounds__(NTHREADS, 2) mega_fwd(KArgs args) {
;     ...
;     if (IN(12)) { moe_tables(F); p12_final(F, args); }
.LBB0_2079:
	s_cmp_lt_i32 s4, 13
	s_cselect_b64 s[0:1], -1, 0
	s_cmp_gt_i32 s5, 12
	s_cselect_b64 s[2:3], -1, 0
	s_and_b64 s[0:1], s[0:1], s[2:3]
	s_andn2_b64 vcc, exec, s[0:1]
	s_cbranch_vccnz .LBB0_2100
	s_cmp_gt_i32 s4, 10
	s_cselect_b32 s2, 64, 0
	v_cmp_gt_u32_e32 vcc, s2, v0
	s_waitcnt vmcnt(0) lgkmcnt(0)
	s_barrier
	s_and_saveexec_b64 s[0:1], vcc
	s_cbranch_execz .LBB0_2097
	v_and_b32_e32 v1, 31, v0
	v_lshlrev_b32_e32 v2, 2, v1
	v_mov_b32_e32 v3, 0
	v_lshl_add_u64 v[2:3], s[72:73], 0, v[2:3]
	v_add_co_u32_e32 v2, vcc, 0x8000, v2
	s_nop 1
	v_addc_co_u32_e32 v3, vcc, 0, v3, vcc
	global_load_dword v3, v[2:3], off sc1
	v_mbcnt_lo_u32_b32 v2, -1, 0
	v_mbcnt_hi_u32_b32 v2, -1, v2
	v_and_b32_e32 v8, 64, v2
	v_add_u32_e32 v4, -1, v2
	v_cmp_lt_i32_e32 vcc, v4, v8
	v_add_u32_e32 v6, -2, v2
	v_add_u32_e32 v7, -4, v2
	v_cndmask_b32_e32 v4, v4, v2, vcc
	v_lshlrev_b32_e32 v4, 2, v4
	v_cmp_lt_i32_e32 vcc, v6, v8
	v_add_u32_e32 v9, -8, v2
	v_add_u32_e32 v11, -16, v2
	v_cndmask_b32_e32 v6, v6, v2, vcc
	v_cmp_ne_u32_e32 vcc, 0, v1
	v_lshlrev_b32_e32 v6, 2, v6
	s_waitcnt vmcnt(0)
	v_add_u32_e32 v5, 0xff, v3
	v_ashrrev_i32_e32 v5, 8, v5
	ds_bpermute_b32 v4, v4, v5
	s_waitcnt lgkmcnt(0)
	v_cndmask_b32_e32 v4, 0, v4, vcc
	v_add_u32_e32 v10, v4, v5
	ds_bpermute_b32 v6, v6, v10
	v_cmp_lt_i32_e32 vcc, v7, v8
	s_nop 1
	v_cndmask_b32_e32 v7, v7, v2, vcc
	v_cmp_lt_u32_e32 vcc, 1, v1
	v_lshlrev_b32_e32 v7, 2, v7
	s_waitcnt lgkmcnt(0)
	v_cndmask_b32_e32 v6, 0, v6, vcc
	v_add_u32_e32 v10, v6, v10
	ds_bpermute_b32 v7, v7, v10
	v_cmp_lt_i32_e32 vcc, v9, v8
	s_nop 1
	v_cndmask_b32_e32 v9, v9, v2, vcc
	v_cmp_lt_u32_e32 vcc, 3, v1
	v_lshlrev_b32_e32 v9, 2, v9
	s_waitcnt lgkmcnt(0)
	v_cndmask_b32_e32 v7, 0, v7, vcc
	v_add_u32_e32 v10, v7, v10
	ds_bpermute_b32 v9, v9, v10
	v_cmp_lt_i32_e32 vcc, v11, v8
	s_nop 1
	v_cndmask_b32_e32 v11, v11, v2, vcc
	v_cmp_lt_u32_e32 vcc, 7, v1
	s_waitcnt lgkmcnt(0)
	s_nop 0
	v_cndmask_b32_e32 v8, 0, v9, vcc
	v_add_u32_e32 v2, v8, v10
	v_lshlrev_b32_e32 v9, 2, v11
	ds_bpermute_b32 v9, v9, v2
	v_cmp_gt_u32_e32 vcc, 32, v0
	s_and_b64 exec, exec, vcc
	s_cbranch_execz .LBB0_2097
	v_cmp_lt_u32_e32 vcc, 15, v1
	v_lshl_add_u32 v10, v1, 2, 0
	v_add_u32_e32 v10, 0x20100, v10
	s_waitcnt lgkmcnt(0)
	v_cndmask_b32_e32 v9, 0, v9, vcc
	v_add_u32_e32 v0, v9, v2
	v_sub_u32_e32 v2, v0, v5
	v_cmp_eq_u32_e32 vcc, 31, v1
	ds_write2_b32 v10, v2, v3 offset1:40
	s_and_saveexec_b64 s[2:3], vcc
	s_add_i32 s4, 0, 0x20180
	v_mov_b32_e32 v3, s4
	ds_write_b32 v3, v0
	s_or_b64 exec, exec, s[2:3]
	v_cmp_lt_i32_e32 vcc, 0, v5
	s_and_b64 exec, exec, vcc
	s_cbranch_execz .LBB0_2097
	v_add3_u32 v3, v4, v6, v7
	v_add3_u32 v3, v3, v8, v9
	v_add_u32_e32 v4, 1, v3
	v_max_i32_e32 v4, v0, v4
	v_sub_u32_e32 v3, v4, v3
	v_cmp_lt_u32_e32 vcc, 1, v3
	s_mov_b64 s[4:5], -1
	s_and_saveexec_b64 s[2:3], vcc
	s_cbranch_execz .LBB0_2094
	v_add_u32_e32 v5, -2, v3
	v_lshrrev_b32_e32 v4, 1, v5
	v_add_u32_e32 v4, 1, v4
	v_cmp_lt_u32_e32 vcc, 13, v5
	v_mov_b32_e32 v7, 0
	s_and_saveexec_b64 s[4:5], vcc
	s_cbranch_execz .LBB0_2090
	v_lshl_add_u32 v6, v2, 2, 0
	v_and_b32_e32 v5, -8, v4
	s_mov_b32 s8, 0
	v_add_u32_e32 v6, 0x20500, v6
	s_mov_b64 s[6:7], 0
